# conversion plan F2: as previous, plus prologue converts layer-1 gate/up experts 12-17 and in-proj-0 converts through expert 11 of layer 1
# baseline (speedup 1.0000x reference)
.LBB0_101:
	s_cmpk_gt_i32 s21, 0xbff
	s_cbranch_scc1 .LBB0_124
	s_ashr_i32 s4, s21, 31
	s_lshr_b32 s2, s4, 24
	s_add_i32 s9, s21, s2
	s_ashr_i32 s2, s9, 8
	s_lshr_b32 s3, s9, 31
	s_add_i32 s3, s2, s3
	s_and_b32 s3, s3, -2
	s_sub_i32 s2, s2, s3
	s_cmp_eq_u32 s2, 1
	s_movk_i32 s8, 0x108
	s_cselect_b32 s3, s8, 0x118
	s_cmp_lg_u32 s2, 0
	s_cselect_b32 s2, s3, 0xf8
	s_add_u32 s2, s0, s2
	s_addc_u32 s3, s1, 0
	s_load_dwordx2 s[2:3], s[2:3], 0x0
	s_lshr_b32 s4, s4, 23
	s_add_i32 s4, s21, s4
	s_ashr_i32 s4, s4, 9
	s_ashr_i32 s5, s4, 31
	s_lshl_b64 s[4:5], s[4:5], 22
	s_load_dwordx2 s[6:7], s[0:1], 0x130
	s_waitcnt lgkmcnt(0)
	s_add_u32 s2, s2, s4
	s_addc_u32 s3, s3, s5
	s_and_b32 s4, s9, 0xff00
	s_sub_i32 s4, s21, s4
	s_sext_i32_i16 s5, s4
	s_bfe_u32 s5, s5, 0x5001a
	s_add_i32 s5, s4, s5
	s_sext_i32_i16 s9, s5
	s_and_b32 s5, s5, 0xffe0
	s_sub_i32 s4, s4, s5
	s_lshl_b32 s5, s9, 2
	s_and_b32 s5, s5, 0xffffff80
	v_and_b32_e32 v132, -16, v143
	s_waitcnt vmcnt(16)
	v_add_u32_e32 v0, s5, v132
	s_sext_i32_i16 s4, s4
	v_ashrrev_i32_e32 v1, 31, v0
	s_lshl_b32 s4, s4, 5
	v_lshlrev_b64 v[0:1], 12, v[0:1]
	v_lshl_add_u64 v[0:1], s[2:3], 0, v[0:1]
	s_ashr_i32 s5, s4, 31
	v_and_b32_e32 v134, 28, v142
	v_lshl_add_u64 v[0:1], s[4:5], 2, v[0:1]
	v_mov_b32_e32 v137, 0
	v_lshlrev_b32_e32 v136, 2, v134
	s_waitcnt vmcnt(5)
	v_lshl_add_u64 v[52:53], v[0:1], 0, v[136:137]
	s_mov_b32 s9, 0xb001000
	v_add_co_u32_e32 v8, vcc, s9, v52
	s_mov_b32 s10, 0xb003000
	s_nop 0
	v_addc_co_u32_e32 v9, vcc, 0, v53, vcc
	v_add_co_u32_e32 v16, vcc, s10, v52
	s_mov_b32 s11, 0xb005000
	s_nop 0
	v_addc_co_u32_e32 v17, vcc, 0, v53, vcc
	v_add_co_u32_e32 v24, vcc, s11, v52
	s_mov_b32 s12, 0xb007000
	s_nop 0
	v_addc_co_u32_e32 v25, vcc, 0, v53, vcc
	v_add_co_u32_e32 v32, vcc, s12, v52
	s_mov_b32 s13, 0xb009000
	s_nop 0
	v_addc_co_u32_e32 v33, vcc, 0, v53, vcc
	v_add_co_u32_e32 v40, vcc, s13, v52
	s_mov_b32 s14, 0xb00b000
	s_nop 0
	v_addc_co_u32_e32 v41, vcc, 0, v53, vcc
	v_add_co_u32_e32 v48, vcc, s14, v52
	s_mov_b32 s2, 0xb00d000
	s_nop 0
	v_addc_co_u32_e32 v49, vcc, 0, v53, vcc
	v_add_co_u32_e32 v54, vcc, s2, v52
	s_mov_b32 s2, 0xb00f000
	s_nop 0
	v_addc_co_u32_e32 v55, vcc, 0, v53, vcc
	v_add_co_u32_e32 v52, vcc, s2, v52
	global_load_dwordx4 v[0:3], v[8:9], off offset:-4096 nt
	global_load_dwordx4 v[4:7], v[8:9], off nt
	v_addc_co_u32_e32 v53, vcc, 0, v53, vcc
	global_load_dwordx4 v[8:11], v[16:17], off offset:-4096 nt
	global_load_dwordx4 v[12:15], v[16:17], off nt
	s_nop 0
	global_load_dwordx4 v[16:19], v[24:25], off offset:-4096 nt
	global_load_dwordx4 v[20:23], v[24:25], off nt
	s_nop 0
	global_load_dwordx4 v[24:27], v[32:33], off offset:-4096 nt
	global_load_dwordx4 v[28:31], v[32:33], off nt
	s_nop 0
	global_load_dwordx4 v[32:35], v[40:41], off offset:-4096 nt
	global_load_dwordx4 v[36:39], v[40:41], off nt
	s_nop 0
	global_load_dwordx4 v[40:43], v[48:49], off offset:-4096 nt
	global_load_dwordx4 v[44:47], v[48:49], off nt
	s_nop 0
	global_load_dwordx4 v[48:51], v[54:55], off offset:-4096 nt
	global_load_dwordx4 v[60:63], v[54:55], off nt
	global_load_dwordx4 v[88:91], v[52:53], off offset:-4096 nt
	global_load_dwordx4 v[92:95], v[52:53], off nt
	s_add_u32 s16, s6, 0x2900000
	v_readlane_b32 s2, v243, 14
	s_mov_b32 s15, 0xb00c000
	s_addc_u32 s17, s7, 0
	v_ashrrev_i32_e32 v133, 31, v132
	s_lshl_b32 s18, s2, 4
	s_mov_b32 s19, 0xc3e00000
	s_mov_b64 s[2:3], 0x200000
	v_mov_b32_e32 v143, 0x43e00000
	v_mov_b32_e32 v144, 0xffffff04
	s_branch .LBB0_105
.LBB0_103:
	s_add_i32 s21, s22, s20
	v_ashrrev_i32_e32 v141, 31, v140
	v_lshlrev_b64 v[140:141], 10, v[140:141]
	s_cmpk_gt_i32 s21, 0xbff
	v_lshl_add_u64 v[138:139], v[138:139], 0, v[140:141]
	s_cselect_b64 s[4:5], -1, 0
	global_store_dwordx4 v[138:139], v[128:131], off

.LBB0_105:
	s_add_i32 s22, s21, s20
	s_cmpk_lt_i32 s22, 0xc00
	s_cselect_b64 s[4:5], -1, 0
	s_cmpk_gt_i32 s22, 0xbff
	s_cbranch_scc1 .LBB0_107
	s_ashr_i32 s23, s22, 31
	s_lshr_b32 s6, s23, 24
	s_add_i32 s26, s22, s6
	s_lshr_b32 s6, s26, 31
	s_ashr_i32 s7, s26, 8
	s_add_i32 s6, s7, s6
	s_and_b32 s6, s6, -2
	s_sub_i32 s6, s7, s6
	s_cmp_eq_u32 s6, 1
	s_cselect_b32 s7, s8, 0x118
	s_cmp_lg_u32 s6, 0
	s_cselect_b32 s6, s7, 0xf8
	s_add_u32 s6, s0, s6
	s_addc_u32 s7, s1, 0
	s_load_dwordx2 s[6:7], s[6:7], 0x0
	s_lshr_b32 s23, s23, 23
	s_add_i32 s23, s22, s23
	s_ashr_i32 s24, s23, 9
	s_ashr_i32 s25, s24, 31
	s_lshl_b64 s[24:25], s[24:25], 22
	s_waitcnt lgkmcnt(0)
	s_add_u32 s6, s6, s24
	s_addc_u32 s7, s7, s25
	s_and_b32 s23, s26, 0xff00
	s_sub_i32 s23, s22, s23
	s_sext_i32_i16 s24, s23
	s_bfe_u32 s24, s24, 0x5001a
	s_add_i32 s24, s23, s24
	s_sext_i32_i16 s25, s24
	s_and_b32 s24, s24, 0xffe0
	s_sub_i32 s23, s23, s24
	s_lshl_b32 s24, s25, 2
	s_and_b32 s25, s24, 0xffffff80
	v_add_u32_e32 v52, s25, v132
	s_sext_i32_i16 s23, s23
	v_ashrrev_i32_e32 v53, 31, v52
	s_lshl_b32 s24, s23, 5
	v_lshlrev_b64 v[52:53], 12, v[52:53]
	v_lshl_add_u64 v[52:53], s[6:7], 0, v[52:53]
	s_ashr_i32 s25, s24, 31
	v_lshl_add_u64 v[52:53], s[24:25], 2, v[52:53]
	v_lshlrev_b32_e32 v136, 2, v134
	v_lshl_add_u64 v[120:121], v[52:53], 0, v[136:137]
	v_add_co_u32_e32 v64, vcc, s9, v120
	s_nop 1
	v_addc_co_u32_e32 v65, vcc, 0, v121, vcc
	s_waitcnt vmcnt(20)
	v_add_co_u32_e32 v72, vcc, s10, v120
	global_load_dwordx4 v[56:59], v[64:65], off offset:-4096 nt
	global_load_dwordx4 v[52:55], v[64:65], off nt
	v_addc_co_u32_e32 v73, vcc, 0, v121, vcc
	v_add_co_u32_e32 v80, vcc, s11, v120
	global_load_dwordx4 v[68:71], v[72:73], off offset:-4096 nt
	global_load_dwordx4 v[64:67], v[72:73], off nt
	v_addc_co_u32_e32 v81, vcc, 0, v121, vcc
	s_waitcnt vmcnt(22)
	v_add_co_u32_e32 v96, vcc, s12, v120
	global_load_dwordx4 v[76:79], v[80:81], off offset:-4096 nt
	global_load_dwordx4 v[72:75], v[80:81], off nt
	v_addc_co_u32_e32 v97, vcc, 0, v121, vcc
	s_waitcnt vmcnt(23)
	v_add_co_u32_e32 v104, vcc, s13, v120
	global_load_dwordx4 v[84:87], v[96:97], off offset:-4096 nt
	global_load_dwordx4 v[80:83], v[96:97], off nt
	v_addc_co_u32_e32 v105, vcc, 0, v121, vcc
	v_add_co_u32_e32 v112, vcc, s14, v120
	global_load_dwordx4 v[100:103], v[104:105], off offset:-4096 nt
	global_load_dwordx4 v[96:99], v[104:105], off nt
	v_addc_co_u32_e32 v113, vcc, 0, v121, vcc
	global_load_dwordx4 v[108:111], v[112:113], off offset:-4096 nt
	global_load_dwordx4 v[104:107], v[112:113], off nt
	v_add_co_u32_e32 v112, vcc, 0xb00c000, v120
	s_nop 1
	v_addc_co_u32_e32 v113, vcc, 0, v121, vcc
	v_add_co_u32_e32 v116, vcc, 0xb00d000, v120
	s_nop 1
	v_addc_co_u32_e32 v117, vcc, 0, v121, vcc
	v_add_co_u32_e32 v122, vcc, 0xb00e000, v120
	global_load_dwordx4 v[112:115], v[112:113], off nt
	s_nop 0
	global_load_dwordx4 v[116:119], v[116:117], off nt
	v_addc_co_u32_e32 v123, vcc, 0, v121, vcc
	v_add_co_u32_e32 v124, vcc, 0xb00f000, v120
	s_nop 1
	v_addc_co_u32_e32 v125, vcc, 0, v121, vcc
	global_load_dwordx4 v[120:123], v[122:123], off nt
	s_nop 0
	global_load_dwordx4 v[124:127], v[124:125], off nt
.LBB0_107:
	s_ashr_i32 s6, s21, 31
	s_lshr_b32 s7, s6, 24
	s_add_i32 s7, s21, s7
	s_lshr_b32 s6, s6, 23
	s_ashr_i32 s24, s7, 8
	s_and_b32 s23, s7, 0xffffff00
	s_add_i32 s6, s21, s6
	s_lshr_b32 s7, s7, 31
	s_ashr_i32 s6, s6, 9
	s_add_i32 s7, s24, s7
	s_add_i32 s6, s6, 44
	s_and_b32 s7, s7, -2
	s_sub_i32 s23, s21, s23
	s_sub_i32 s26, s24, s7
	s_mul_hi_i32 s7, s6, 0x300000
	s_mul_i32 s6, s6, 0x300000
	s_add_u32 s24, s16, s6
	s_addc_u32 s25, s17, s7
	s_mov_b64 s[6:7], -1
	s_cmp_gt_i32 s26, 0
	s_waitcnt vmcnt(15)
	v_mul_f32_e32 v203, 0x42000000, v0
	s_waitcnt vmcnt(14)
	v_mul_f32_e32 v204, 0x42000000, v4
	s_waitcnt vmcnt(13)
	v_mul_f32_e32 v205, 0x42000000, v8
	s_waitcnt vmcnt(12)
	v_mul_f32_e32 v206, 0x42000000, v12
	s_waitcnt vmcnt(11)
	v_mul_f32_e32 v201, 0x42000000, v16
	s_waitcnt vmcnt(10)
	v_mul_f32_e32 v202, 0x42000000, v20
	s_waitcnt vmcnt(9)
	v_mul_f32_e32 v199, 0x42000000, v24
	s_waitcnt vmcnt(8)
	v_mul_f32_e32 v200, 0x42000000, v28
	s_waitcnt vmcnt(7)
	v_mul_f32_e32 v195, 0x42000000, v32
	s_waitcnt vmcnt(6)
	v_mul_f32_e32 v196, 0x42000000, v36
	s_waitcnt vmcnt(5)
	v_mul_f32_e32 v197, 0x42000000, v40
	s_waitcnt vmcnt(4)
	v_mul_f32_e32 v198, 0x42000000, v44
	s_waitcnt vmcnt(3)
	v_mul_f32_e32 v193, 0x42000000, v48
	s_waitcnt vmcnt(2)
	v_mul_f32_e32 v194, 0x42000000, v60
	s_waitcnt vmcnt(1)
	v_mul_f32_e32 v191, 0x42000000, v88
	s_waitcnt vmcnt(0)
	v_mul_f32_e32 v192, 0x42000000, v92
	v_mul_f32_e32 v187, 0x42000000, v1
	v_mul_f32_e32 v188, 0x42000000, v5
	v_mul_f32_e32 v189, 0x42000000, v9
	v_mul_f32_e32 v190, 0x42000000, v13
	v_mul_f32_e32 v185, 0x42000000, v17
	v_mul_f32_e32 v186, 0x42000000, v21
	v_mul_f32_e32 v183, 0x42000000, v25
	v_mul_f32_e32 v184, 0x42000000, v29
	v_mul_f32_e32 v179, 0x42000000, v33
	v_mul_f32_e32 v180, 0x42000000, v37
	v_mul_f32_e32 v181, 0x42000000, v41
	v_mul_f32_e32 v182, 0x42000000, v45
	v_mul_f32_e32 v177, 0x42000000, v49
	v_mul_f32_e32 v178, 0x42000000, v61
	v_mul_f32_e32 v175, 0x42000000, v89
	v_mul_f32_e32 v176, 0x42000000, v93
	v_mul_f32_e32 v171, 0x42000000, v2
	v_mul_f32_e32 v172, 0x42000000, v6
	v_mul_f32_e32 v173, 0x42000000, v10
	v_mul_f32_e32 v174, 0x42000000, v14
	v_mul_f32_e32 v169, 0x42000000, v18
	v_mul_f32_e32 v170, 0x42000000, v22
	v_mul_f32_e32 v167, 0x42000000, v26
	v_mul_f32_e32 v168, 0x42000000, v30
	v_mul_f32_e32 v163, 0x42000000, v34
	v_mul_f32_e32 v164, 0x42000000, v38
	v_mul_f32_e32 v165, 0x42000000, v42
	v_mul_f32_e32 v166, 0x42000000, v46
	v_mul_f32_e32 v161, 0x42000000, v50
	v_mul_f32_e32 v162, 0x42000000, v62
	v_mul_f32_e32 v159, 0x42000000, v90
	v_mul_f32_e32 v160, 0x42000000, v94
	v_mul_f32_e32 v155, 0x42000000, v3
	v_mul_f32_e32 v156, 0x42000000, v7
	v_mul_f32_e32 v157, 0x42000000, v11
	v_mul_f32_e32 v158, 0x42000000, v15
	v_mul_f32_e32 v153, 0x42000000, v19
	v_mul_f32_e32 v154, 0x42000000, v23
	v_mul_f32_e32 v151, 0x42000000, v27
	v_mul_f32_e32 v152, 0x42000000, v31
	v_mul_f32_e32 v147, 0x42000000, v35
	v_mul_f32_e32 v148, 0x42000000, v39
	v_mul_f32_e32 v149, 0x42000000, v43
	v_mul_f32_e32 v150, 0x42000000, v47
	v_mul_f32_e32 v145, 0x42000000, v51
	v_mul_f32_e32 v146, 0x42000000, v63
	v_mul_f32_e32 v136, 0x42000000, v91
	v_mul_f32_e32 v141, 0x42000000, v95
	s_cbranch_scc0 .LBB0_109
	v_med3_f32 v129, v203, s19, v143
	v_med3_f32 v130, v204, s19, v143
	v_mov_b32_e32 v128, v137
	v_cvt_pk_fp8_f32 v128, v129, v130
	v_med3_f32 v130, v201, s19, v143
	v_med3_f32 v208, v202, s19, v143
	v_mov_b32_e32 v129, v137
	v_cvt_pk_fp8_f32 v129, v130, v208
	s_bfe_u32 s6, s23, 0x5001a
	s_add_i32 s6, s23, s6
	v_med3_f32 v131, v205, s19, v143
	v_med3_f32 v207, v206, s19, v143
	s_sext_i32_i16 s7, s6
	s_and_b32 s6, s6, 0xffe0
	v_cvt_pk_fp8_f32 v128, v131, v207 op_sel:[0,0,1]
	v_med3_f32 v130, v199, s19, v143
	v_med3_f32 v131, v200, s19, v143
	s_sub_i32 s6, s23, s6
	v_cvt_pk_fp8_f32 v129, v130, v131 op_sel:[0,0,1]
	v_med3_f32 v131, v195, s19, v143
	v_med3_f32 v207, v196, s19, v143
	v_mov_b32_e32 v130, v137
	s_sext_i32_i16 s6, s6
	v_cvt_pk_fp8_f32 v130, v131, v207
	v_med3_f32 v207, v193, s19, v143
	v_med3_f32 v210, v194, s19, v143
	v_mov_b32_e32 v131, v137
	s_lshl_b32 s27, s6, 5
	s_lshl_b32 s6, s6, 6
	v_cvt_pk_fp8_f32 v131, v207, v210
	s_lshl_b32 s7, s7, 2
	s_and_b32 s6, s6, 0xffffff00
	s_and_b32 s27, s27, 0x60
	s_and_b32 s7, s7, 0xffffff80
	s_or_b32 s6, s27, s6
	v_med3_f32 v208, v197, s19, v143
	v_med3_f32 v209, v198, s19, v143
	v_or_b32_e32 v140, s6, v134
	s_ashr_i32 s27, s7, 31
	v_cvt_pk_fp8_f32 v130, v208, v209 op_sel:[0,0,1]
	v_med3_f32 v207, v191, s19, v143
	v_med3_f32 v208, v192, s19, v143
	s_add_u32 s6, s24, s7
	v_cvt_pk_fp8_f32 v131, v207, v208 op_sel:[0,0,1]
	v_or_b32_e32 v208, 0x80, v140
	s_addc_u32 s7, s25, s27
	v_ashrrev_i32_e32 v209, 31, v208
	v_lshl_add_u64 v[138:139], s[6:7], 0, v[132:133]
	v_lshlrev_b64 v[208:209], 10, v[208:209]
	v_lshl_add_u64 v[208:209], v[138:139], 0, v[208:209]
	global_store_dwordx4 v[208:209], v[128:131], off
	v_med3_f32 v208, v186, s19, v143
	v_med3_f32 v207, v190, s19, v143
	v_med3_f32 v129, v187, s19, v143
	v_med3_f32 v130, v188, s19, v143
	v_mov_b32_e32 v128, v137
	v_cvt_pk_fp8_f32 v128, v129, v130
	v_med3_f32 v130, v185, s19, v143
	v_mov_b32_e32 v129, v137
	v_cvt_pk_fp8_f32 v129, v130, v208
	v_med3_f32 v131, v189, s19, v143
	v_cvt_pk_fp8_f32 v128, v131, v207 op_sel:[0,0,1]
	v_med3_f32 v130, v183, s19, v143
	v_med3_f32 v131, v184, s19, v143
	v_cvt_pk_fp8_f32 v129, v130, v131 op_sel:[0,0,1]
	v_med3_f32 v131, v179, s19, v143
	v_med3_f32 v207, v180, s19, v143
	v_mov_b32_e32 v130, v137
	v_cvt_pk_fp8_f32 v130, v131, v207
	v_med3_f32 v207, v177, s19, v143
	v_med3_f32 v210, v178, s19, v143
	v_mov_b32_e32 v131, v137
	v_cvt_pk_fp8_f32 v131, v207, v210
	v_med3_f32 v208, v181, s19, v143
	v_med3_f32 v209, v182, s19, v143
	v_cvt_pk_fp8_f32 v130, v208, v209 op_sel:[0,0,1]
	v_med3_f32 v207, v175, s19, v143
	v_med3_f32 v208, v176, s19, v143
	v_cvt_pk_fp8_f32 v131, v207, v208 op_sel:[0,0,1]
	v_or_b32_e32 v208, 0x81, v140
	v_ashrrev_i32_e32 v209, 31, v208
	v_lshlrev_b64 v[208:209], 10, v[208:209]
	v_lshl_add_u64 v[208:209], v[138:139], 0, v[208:209]
	global_store_dwordx4 v[208:209], v[128:131], off
	v_mov_b32_e32 v208, v137
	v_mov_b32_e32 v209, v137
	v_med3_f32 v128, v171, s19, v143
	v_med3_f32 v129, v172, s19, v143
	v_cvt_pk_fp8_f32 v208, v128, v129
	v_med3_f32 v128, v169, s19, v143
	v_med3_f32 v129, v170, s19, v143
	v_cvt_pk_fp8_f32 v209, v128, v129
	v_med3_f32 v128, v167, s19, v143
	v_med3_f32 v129, v168, s19, v143
	v_mov_b32_e32 v210, v137
	v_cvt_pk_fp8_f32 v209, v128, v129 op_sel:[0,0,1]
	v_med3_f32 v128, v163, s19, v143
	v_med3_f32 v129, v164, s19, v143
	v_cvt_pk_fp8_f32 v210, v128, v129
	v_med3_f32 v128, v161, s19, v143
	v_med3_f32 v129, v162, s19, v143
	v_mov_b32_e32 v211, v137
	v_cvt_pk_fp8_f32 v211, v128, v129
	v_med3_f32 v128, v159, s19, v143
	v_med3_f32 v129, v160, s19, v143
	v_med3_f32 v130, v173, s19, v143
	v_cvt_pk_fp8_f32 v211, v128, v129 op_sel:[0,0,1]
	v_or_b32_e32 v128, 0x82, v140
	v_med3_f32 v131, v174, s19, v143
	v_ashrrev_i32_e32 v129, 31, v128
	v_cvt_pk_fp8_f32 v208, v130, v131 op_sel:[0,0,1]
	v_med3_f32 v130, v165, s19, v143
	v_med3_f32 v131, v166, s19, v143
	v_lshlrev_b64 v[128:129], 10, v[128:129]
	v_cvt_pk_fp8_f32 v210, v130, v131 op_sel:[0,0,1]
	v_lshl_add_u64 v[212:213], v[138:139], 0, v[128:129]
	v_med3_f32 v129, v155, s19, v143
	v_med3_f32 v130, v156, s19, v143
	v_mov_b32_e32 v128, v137
	v_cvt_pk_fp8_f32 v128, v129, v130
	v_med3_f32 v130, v153, s19, v143
	v_med3_f32 v214, v154, s19, v143
	v_mov_b32_e32 v129, v137
	v_cvt_pk_fp8_f32 v129, v130, v214
	v_med3_f32 v131, v157, s19, v143
	v_med3_f32 v207, v158, s19, v143
	v_cvt_pk_fp8_f32 v128, v131, v207 op_sel:[0,0,1]
	v_med3_f32 v130, v151, s19, v143
	v_med3_f32 v131, v152, s19, v143
	v_cvt_pk_fp8_f32 v129, v130, v131 op_sel:[0,0,1]
	v_med3_f32 v131, v147, s19, v143
	v_med3_f32 v207, v148, s19, v143
	v_mov_b32_e32 v130, v137
	v_cvt_pk_fp8_f32 v130, v131, v207
	v_med3_f32 v207, v145, s19, v143
	v_med3_f32 v216, v146, s19, v143
	v_mov_b32_e32 v131, v137
	v_cvt_pk_fp8_f32 v131, v207, v216
	v_med3_f32 v214, v149, s19, v143
	v_med3_f32 v215, v150, s19, v143
	v_cvt_pk_fp8_f32 v130, v214, v215 op_sel:[0,0,1]
	v_med3_f32 v207, v136, s19, v143
	v_med3_f32 v214, v141, s19, v143
	v_cvt_pk_fp8_f32 v131, v207, v214 op_sel:[0,0,1]
	global_store_dwordx4 v[212:213], v[208:211], off
	v_or_b32_e32 v140, 0x83, v140
	s_mov_b64 s[6:7], 0

.LBB0_113:
	v_ashrrev_i32_e32 v141, 31, v140
	v_lshlrev_b64 v[140:141], 10, v[140:141]
	v_lshl_add_u64 v[138:139], v[138:139], 0, v[140:141]
	s_andn2_b64 vcc, exec, s[4:5]
	s_mov_b64 s[4:5], -1
	global_store_dwordx4 v[138:139], v[128:131], off
	s_cbranch_vccnz .LBB0_104
	s_add_i32 s4, s18, s21
	s_cmpk_gt_i32 s4, 0xbff
	s_cbranch_scc1 .LBB0_116
	s_ashr_i32 s5, s4, 31
	s_lshr_b32 s6, s5, 24
	s_add_i32 s21, s4, s6
	s_ashr_i32 s6, s21, 8
	s_lshr_b32 s7, s21, 31
	s_add_i32 s7, s6, s7
	s_and_b32 s7, s7, -2
	s_sub_i32 s6, s6, s7
	s_cmp_eq_u32 s6, 1
	s_cselect_b32 s7, s8, 0x118
	s_cmp_lg_u32 s6, 0
	s_cselect_b32 s6, s7, 0xf8
	s_add_u32 s6, s0, s6
	s_addc_u32 s7, s1, 0
	s_load_dwordx2 s[6:7], s[6:7], 0x0
	s_lshr_b32 s5, s5, 23
	s_add_i32 s5, s4, s5
	s_ashr_i32 s24, s5, 9
	s_ashr_i32 s25, s24, 31
	s_lshl_b64 s[24:25], s[24:25], 22
	s_waitcnt lgkmcnt(0)
	s_add_u32 s6, s6, s24
	s_addc_u32 s7, s7, s25
	s_and_b32 s5, s21, 0xff00
	s_sub_i32 s4, s4, s5
	s_sext_i32_i16 s5, s4
	s_bfe_u32 s5, s5, 0x5001a
	s_add_i32 s5, s4, s5
	s_sext_i32_i16 s21, s5
	s_and_b32 s5, s5, 0xffe0
	s_sub_i32 s4, s4, s5
	s_lshl_b32 s5, s21, 2
	s_and_b32 s5, s5, 0xffffff80
	v_add_u32_e32 v0, s5, v132
	s_sext_i32_i16 s4, s4
	v_ashrrev_i32_e32 v1, 31, v0
	s_lshl_b32 s4, s4, 5
	v_lshlrev_b64 v[0:1], 12, v[0:1]
	v_lshl_add_u64 v[0:1], s[6:7], 0, v[0:1]
	s_ashr_i32 s5, s4, 31
	v_lshl_add_u64 v[0:1], s[4:5], 2, v[0:1]
	v_lshlrev_b32_e32 v136, 2, v134
	v_lshl_add_u64 v[88:89], v[0:1], 0, v[136:137]
	v_add_co_u32_e32 v8, vcc, s9, v88
	s_nop 1
	v_addc_co_u32_e32 v9, vcc, 0, v89, vcc
	v_add_co_u32_e32 v16, vcc, s10, v88
	global_load_dwordx4 v[0:3], v[8:9], off offset:-4096 nt
	global_load_dwordx4 v[4:7], v[8:9], off nt
	v_addc_co_u32_e32 v17, vcc, 0, v89, vcc
	v_add_co_u32_e32 v24, vcc, s11, v88
	global_load_dwordx4 v[8:11], v[16:17], off offset:-4096 nt
	global_load_dwordx4 v[12:15], v[16:17], off nt
	v_addc_co_u32_e32 v25, vcc, 0, v89, vcc
	v_add_co_u32_e32 v32, vcc, s12, v88
	global_load_dwordx4 v[16:19], v[24:25], off offset:-4096 nt
	global_load_dwordx4 v[20:23], v[24:25], off nt
	v_addc_co_u32_e32 v33, vcc, 0, v89, vcc
	v_add_co_u32_e32 v40, vcc, s13, v88
	global_load_dwordx4 v[24:27], v[32:33], off offset:-4096 nt
	global_load_dwordx4 v[28:31], v[32:33], off nt
	v_addc_co_u32_e32 v41, vcc, 0, v89, vcc
	v_add_co_u32_e32 v48, vcc, s14, v88
	global_load_dwordx4 v[32:35], v[40:41], off offset:-4096 nt
	global_load_dwordx4 v[36:39], v[40:41], off nt
	v_addc_co_u32_e32 v49, vcc, 0, v89, vcc
	global_load_dwordx4 v[40:43], v[48:49], off offset:-4096 nt
	global_load_dwordx4 v[44:47], v[48:49], off nt
	v_add_co_u32_e32 v48, vcc, s15, v88
	s_nop 1
	v_addc_co_u32_e32 v49, vcc, 0, v89, vcc
	v_add_co_u32_e32 v60, vcc, 0xb00d000, v88
	s_nop 1
	v_addc_co_u32_e32 v61, vcc, 0, v89, vcc
	v_add_co_u32_e32 v90, vcc, 0xb00e000, v88
	global_load_dwordx4 v[48:51], v[48:49], off nt
	s_nop 0
	global_load_dwordx4 v[60:63], v[60:61], off nt
	v_addc_co_u32_e32 v91, vcc, 0, v89, vcc
	v_add_co_u32_e32 v92, vcc, 0xb00f000, v88
	s_nop 1
	v_addc_co_u32_e32 v93, vcc, 0, v89, vcc
	global_load_dwordx4 v[88:91], v[90:91], off nt
	s_nop 0
	global_load_dwordx4 v[92:95], v[92:93], off nt
.LBB0_116:
	s_ashr_i32 s4, s22, 31
	s_lshr_b32 s5, s4, 24
	s_add_i32 s5, s22, s5
	s_lshr_b32 s4, s4, 23
	s_ashr_i32 s7, s5, 8
	s_and_b32 s6, s5, 0xffffff00
	s_add_i32 s4, s22, s4
	s_lshr_b32 s5, s5, 31
	s_ashr_i32 s4, s4, 9
	s_add_i32 s5, s7, s5
	s_add_i32 s4, s4, 44
	s_and_b32 s5, s5, -2
	s_sub_i32 s6, s22, s6
	s_sub_i32 s23, s7, s5
	s_mul_hi_i32 s5, s4, 0x300000
	s_mul_i32 s4, s4, 0x300000
	s_add_u32 s7, s16, s4
	s_addc_u32 s21, s17, s5
	s_mov_b64 s[4:5], -1
	s_cmp_gt_i32 s23, 0
	v_mul_f32_e32 v203, 0x42000000, v56
	v_mul_f32_e32 v204, 0x42000000, v52
	v_mul_f32_e32 v205, 0x42000000, v68
	v_mul_f32_e32 v206, 0x42000000, v64
	v_mul_f32_e32 v201, 0x42000000, v76
	v_mul_f32_e32 v202, 0x42000000, v72
	v_mul_f32_e32 v199, 0x42000000, v84
	v_mul_f32_e32 v200, 0x42000000, v80
	v_mul_f32_e32 v195, 0x42000000, v100
	v_mul_f32_e32 v196, 0x42000000, v96
	v_mul_f32_e32 v197, 0x42000000, v108
	v_mul_f32_e32 v198, 0x42000000, v104
	v_mul_f32_e32 v193, 0x42000000, v112
	v_mul_f32_e32 v194, 0x42000000, v116
	v_mul_f32_e32 v191, 0x42000000, v120
	v_mul_f32_e32 v192, 0x42000000, v124
	v_mul_f32_e32 v187, 0x42000000, v57
	v_mul_f32_e32 v188, 0x42000000, v53
	v_mul_f32_e32 v189, 0x42000000, v69
	v_mul_f32_e32 v190, 0x42000000, v65
	v_mul_f32_e32 v185, 0x42000000, v77
	v_mul_f32_e32 v186, 0x42000000, v73
	v_mul_f32_e32 v183, 0x42000000, v85
	v_mul_f32_e32 v184, 0x42000000, v81
	v_mul_f32_e32 v179, 0x42000000, v101
	v_mul_f32_e32 v180, 0x42000000, v97
	v_mul_f32_e32 v181, 0x42000000, v109
	v_mul_f32_e32 v182, 0x42000000, v105
	v_mul_f32_e32 v177, 0x42000000, v113
	v_mul_f32_e32 v178, 0x42000000, v117
	v_mul_f32_e32 v175, 0x42000000, v121
	v_mul_f32_e32 v176, 0x42000000, v125
	v_mul_f32_e32 v171, 0x42000000, v58
	v_mul_f32_e32 v172, 0x42000000, v54
	v_mul_f32_e32 v173, 0x42000000, v70
	v_mul_f32_e32 v174, 0x42000000, v66
	v_mul_f32_e32 v169, 0x42000000, v78
	v_mul_f32_e32 v170, 0x42000000, v74
	v_mul_f32_e32 v167, 0x42000000, v86
	v_mul_f32_e32 v168, 0x42000000, v82
	v_mul_f32_e32 v163, 0x42000000, v102
	v_mul_f32_e32 v164, 0x42000000, v98
	v_mul_f32_e32 v165, 0x42000000, v110
	v_mul_f32_e32 v166, 0x42000000, v106
	v_mul_f32_e32 v161, 0x42000000, v114
	v_mul_f32_e32 v162, 0x42000000, v118
	v_mul_f32_e32 v159, 0x42000000, v122
	v_mul_f32_e32 v160, 0x42000000, v126
	v_mul_f32_e32 v155, 0x42000000, v59
	v_mul_f32_e32 v156, 0x42000000, v55
	v_mul_f32_e32 v157, 0x42000000, v71
	v_mul_f32_e32 v158, 0x42000000, v67
	v_mul_f32_e32 v153, 0x42000000, v79
	v_mul_f32_e32 v154, 0x42000000, v75
	v_mul_f32_e32 v151, 0x42000000, v87
	v_mul_f32_e32 v152, 0x42000000, v83
	v_mul_f32_e32 v147, 0x42000000, v103
	v_mul_f32_e32 v148, 0x42000000, v99
	v_mul_f32_e32 v149, 0x42000000, v111
	v_mul_f32_e32 v150, 0x42000000, v107
	v_mul_f32_e32 v145, 0x42000000, v115
	v_mul_f32_e32 v146, 0x42000000, v119
	v_mul_f32_e32 v136, 0x42000000, v123
	v_mul_f32_e32 v141, 0x42000000, v127
	s_cbranch_scc0 .LBB0_118
	v_med3_f32 v129, v203, s19, v143
	v_med3_f32 v130, v204, s19, v143
	v_mov_b32_e32 v128, v137
	v_cvt_pk_fp8_f32 v128, v129, v130
	v_med3_f32 v130, v201, s19, v143
	v_med3_f32 v208, v202, s19, v143
	v_mov_b32_e32 v129, v137
	v_cvt_pk_fp8_f32 v129, v130, v208
	s_bfe_u32 s4, s6, 0x5001a
	s_add_i32 s4, s6, s4
	v_med3_f32 v131, v205, s19, v143
	v_med3_f32 v207, v206, s19, v143
	s_sext_i32_i16 s5, s4
	s_and_b32 s4, s4, 0xffe0
	v_cvt_pk_fp8_f32 v128, v131, v207 op_sel:[0,0,1]
	v_med3_f32 v130, v199, s19, v143
	v_med3_f32 v131, v200, s19, v143
	s_sub_i32 s4, s6, s4
	v_cvt_pk_fp8_f32 v129, v130, v131 op_sel:[0,0,1]
	v_med3_f32 v131, v195, s19, v143
	v_med3_f32 v207, v196, s19, v143
	v_mov_b32_e32 v130, v137
	s_sext_i32_i16 s4, s4
	v_cvt_pk_fp8_f32 v130, v131, v207
	v_med3_f32 v207, v193, s19, v143
	v_med3_f32 v210, v194, s19, v143
	v_mov_b32_e32 v131, v137
	s_lshl_b32 s24, s4, 5
	s_lshl_b32 s4, s4, 6
	v_cvt_pk_fp8_f32 v131, v207, v210
	s_lshl_b32 s5, s5, 2
	s_and_b32 s4, s4, 0xffffff00
	s_and_b32 s24, s24, 0x60
	s_and_b32 s5, s5, 0xffffff80
	s_or_b32 s4, s24, s4
	v_med3_f32 v208, v197, s19, v143
	v_med3_f32 v209, v198, s19, v143
	v_or_b32_e32 v140, s4, v134
	s_ashr_i32 s24, s5, 31
	v_cvt_pk_fp8_f32 v130, v208, v209 op_sel:[0,0,1]
	v_med3_f32 v207, v191, s19, v143
	v_med3_f32 v208, v192, s19, v143
	s_add_u32 s4, s7, s5
	v_cvt_pk_fp8_f32 v131, v207, v208 op_sel:[0,0,1]
	v_or_b32_e32 v208, 0x80, v140
	s_addc_u32 s5, s21, s24
	v_ashrrev_i32_e32 v209, 31, v208
	v_lshl_add_u64 v[138:139], s[4:5], 0, v[132:133]
	v_lshlrev_b64 v[208:209], 10, v[208:209]
	v_lshl_add_u64 v[208:209], v[138:139], 0, v[208:209]
	global_store_dwordx4 v[208:209], v[128:131], off
	v_med3_f32 v208, v186, s19, v143
	v_med3_f32 v207, v190, s19, v143
	v_med3_f32 v129, v187, s19, v143
	v_med3_f32 v130, v188, s19, v143
	v_mov_b32_e32 v128, v137
	v_cvt_pk_fp8_f32 v128, v129, v130
	v_med3_f32 v130, v185, s19, v143
	v_mov_b32_e32 v129, v137
	v_cvt_pk_fp8_f32 v129, v130, v208
	v_med3_f32 v131, v189, s19, v143
	v_cvt_pk_fp8_f32 v128, v131, v207 op_sel:[0,0,1]
	v_med3_f32 v130, v183, s19, v143
	v_med3_f32 v131, v184, s19, v143
	v_cvt_pk_fp8_f32 v129, v130, v131 op_sel:[0,0,1]
	v_med3_f32 v131, v179, s19, v143
	v_med3_f32 v207, v180, s19, v143
	v_mov_b32_e32 v130, v137
	v_cvt_pk_fp8_f32 v130, v131, v207
	v_med3_f32 v207, v177, s19, v143
	v_med3_f32 v210, v178, s19, v143
	v_mov_b32_e32 v131, v137
	v_cvt_pk_fp8_f32 v131, v207, v210
	v_med3_f32 v208, v181, s19, v143
	v_med3_f32 v209, v182, s19, v143
	v_cvt_pk_fp8_f32 v130, v208, v209 op_sel:[0,0,1]
	v_med3_f32 v207, v175, s19, v143
	v_med3_f32 v208, v176, s19, v143
	v_cvt_pk_fp8_f32 v131, v207, v208 op_sel:[0,0,1]
	v_or_b32_e32 v208, 0x81, v140
	v_ashrrev_i32_e32 v209, 31, v208
	v_lshlrev_b64 v[208:209], 10, v[208:209]
	v_lshl_add_u64 v[208:209], v[138:139], 0, v[208:209]
	global_store_dwordx4 v[208:209], v[128:131], off
	v_mov_b32_e32 v208, v137
	v_mov_b32_e32 v209, v137
	v_med3_f32 v128, v171, s19, v143
	v_med3_f32 v129, v172, s19, v143
	v_cvt_pk_fp8_f32 v208, v128, v129
	v_med3_f32 v128, v169, s19, v143
	v_med3_f32 v129, v170, s19, v143
	v_cvt_pk_fp8_f32 v209, v128, v129
	v_med3_f32 v128, v167, s19, v143
	v_med3_f32 v129, v168, s19, v143
	v_mov_b32_e32 v210, v137
	v_cvt_pk_fp8_f32 v209, v128, v129 op_sel:[0,0,1]
	v_med3_f32 v128, v163, s19, v143
	v_med3_f32 v129, v164, s19, v143
	v_cvt_pk_fp8_f32 v210, v128, v129
	v_med3_f32 v128, v161, s19, v143
	v_med3_f32 v129, v162, s19, v143
	v_mov_b32_e32 v211, v137
	v_cvt_pk_fp8_f32 v211, v128, v129
	v_med3_f32 v128, v159, s19, v143
	v_med3_f32 v129, v160, s19, v143
	v_med3_f32 v130, v173, s19, v143
	v_cvt_pk_fp8_f32 v211, v128, v129 op_sel:[0,0,1]
	v_or_b32_e32 v128, 0x82, v140
	v_med3_f32 v131, v174, s19, v143
	v_ashrrev_i32_e32 v129, 31, v128
	v_cvt_pk_fp8_f32 v208, v130, v131 op_sel:[0,0,1]
	v_med3_f32 v130, v165, s19, v143
	v_med3_f32 v131, v166, s19, v143
	v_lshlrev_b64 v[128:129], 10, v[128:129]
	v_cvt_pk_fp8_f32 v210, v130, v131 op_sel:[0,0,1]
	v_lshl_add_u64 v[212:213], v[138:139], 0, v[128:129]
	v_med3_f32 v129, v155, s19, v143
	v_med3_f32 v130, v156, s19, v143
	v_mov_b32_e32 v128, v137
	v_cvt_pk_fp8_f32 v128, v129, v130
	v_med3_f32 v130, v153, s19, v143
	v_med3_f32 v214, v154, s19, v143
	v_mov_b32_e32 v129, v137
	v_cvt_pk_fp8_f32 v129, v130, v214
	v_med3_f32 v131, v157, s19, v143
	v_med3_f32 v207, v158, s19, v143
	v_cvt_pk_fp8_f32 v128, v131, v207 op_sel:[0,0,1]
	v_med3_f32 v130, v151, s19, v143
	v_med3_f32 v131, v152, s19, v143
	v_cvt_pk_fp8_f32 v129, v130, v131 op_sel:[0,0,1]
	v_med3_f32 v131, v147, s19, v143
	v_med3_f32 v207, v148, s19, v143
	v_mov_b32_e32 v130, v137
	v_cvt_pk_fp8_f32 v130, v131, v207
	v_med3_f32 v207, v145, s19, v143
	v_med3_f32 v216, v146, s19, v143
	v_mov_b32_e32 v131, v137
	v_cvt_pk_fp8_f32 v131, v207, v216
	v_med3_f32 v214, v149, s19, v143
	v_med3_f32 v215, v150, s19, v143
	v_cvt_pk_fp8_f32 v130, v214, v215 op_sel:[0,0,1]
	v_med3_f32 v207, v136, s19, v143
	v_med3_f32 v214, v141, s19, v143
	v_cvt_pk_fp8_f32 v131, v207, v214 op_sel:[0,0,1]
	global_store_dwordx4 v[212:213], v[208:211], off
	v_or_b32_e32 v140, 0x83, v140
	s_mov_b64 s[4:5], 0

.LBB0_254:
	s_load_dwordx4 s[0:3], s[8:9], 0x138
	s_waitcnt lgkmcnt(0)
	s_mov_b64 s[4:5], s[0:1]
	s_cmp_lt_i32 s4, 3
	s_cselect_b64 s[0:1], -1, 0
	s_cmp_gt_i32 s5, 2
	s_cselect_b64 s[2:3], -1, 0
	s_and_b64 s[0:1], s[0:1], s[2:3]
	s_andn2_b64 vcc, exec, s[0:1]
	s_cbranch_vccnz .LBB0_356
	s_mov_b64 s[0:1], s[8:9]
	v_mbcnt_lo_u32_b32 v152, -1, 0
	v_mbcnt_hi_u32_b32 v152, -1, v152
	s_load_dword s38, s[8:9], 0x148
	s_add_u32 s2, s8, 0x148
	v_readlane_b32 s4, v243, 0
	s_addc_u32 s3, s9, 0
	v_readlane_b32 s5, v243, 1
	s_waitcnt lgkmcnt(0)
	s_sub_i32 s39, s38, 40
	s_cmp_lt_i32 s4, s39
	s_mov_b64 s[4:5], -1
	s_cbranch_scc1 .LBB0_276
	v_readlane_b32 s4, v243, 0
	s_sub_i32 s4, s4, s39
	s_lshl_b32 s6, s4, 3
	s_add_i32 s6, s6, s94
	s_cmpk_gt_u32 s6, 0x2fff
	v_readlane_b32 s5, v243, 1
	s_cbranch_scc1 .LBB0_275
	s_bitcmp0_b32 s6, 8
	s_movk_i32 s12, 0xf8
	s_cselect_b32 s4, s12, 0x108
	s_add_u32 s4, s0, s4
	s_addc_u32 s5, s1, 0
	s_load_dwordx2 s[8:9], s[4:5], 0x0
	s_load_dwordx2 s[10:11], s[0:1], 0x130
	s_lshl_b32 s4, s6, 13
	s_and_b32 s4, s4, 0x7c00000
	v_lshlrev_b32_e32 v0, 1, v152
	s_waitcnt lgkmcnt(0)
	s_add_u32 s8, s8, s4
	s_addc_u32 s9, s9, 0
	s_lshl_b32 s4, s6, 2
	s_and_b32 s4, s4, 0x380
	v_and_b32_e32 v132, -16, v0
	v_add_u32_e32 v0, s4, v132
	v_ashrrev_i32_e32 v1, 31, v0
	v_lshlrev_b64 v[0:1], 12, v[0:1]
	s_lshl_b32 s4, s6, 7
	v_lshlrev_b32_e32 v2, 2, v152
	s_mov_b32 s5, 0
	v_lshl_add_u64 v[0:1], s[8:9], 0, v[0:1]
	s_and_b32 s4, s4, 0xf80
	v_and_b32_e32 v134, 28, v2
	v_lshl_add_u64 v[0:1], v[0:1], 0, s[4:5]
	v_mov_b32_e32 v137, 0
	v_lshlrev_b32_e32 v136, 2, v134
	v_lshl_add_u64 v[56:57], v[0:1], 0, v[136:137]
	s_mov_b32 s4, 0x5001000
	v_add_co_u32_e32 v4, vcc, s4, v56
	s_mov_b32 s4, 0x5003000
	s_nop 0
	v_addc_co_u32_e32 v5, vcc, 0, v57, vcc
	v_add_co_u32_e32 v12, vcc, s4, v56
	s_mov_b32 s4, 0x5005000
	s_nop 0
	v_addc_co_u32_e32 v13, vcc, 0, v57, vcc
	v_add_co_u32_e32 v20, vcc, s4, v56
	s_mov_b32 s4, 0x5007000
	s_nop 0
	v_addc_co_u32_e32 v21, vcc, 0, v57, vcc
	v_add_co_u32_e32 v32, vcc, s4, v56
	s_mov_b32 s4, 0x5009000
	s_nop 0
	v_addc_co_u32_e32 v33, vcc, 0, v57, vcc
	v_add_co_u32_e32 v40, vcc, s4, v56
	s_mov_b32 s4, 0x500b000
	s_nop 0
	v_addc_co_u32_e32 v41, vcc, 0, v57, vcc
	v_add_co_u32_e32 v48, vcc, s4, v56
	s_mov_b32 s4, 0x500d000
	s_nop 0
	v_addc_co_u32_e32 v49, vcc, 0, v57, vcc
	v_add_co_u32_e32 v58, vcc, s4, v56
	s_mov_b32 s4, 0x500f000
	s_nop 0
	v_addc_co_u32_e32 v59, vcc, 0, v57, vcc
	v_add_co_u32_e32 v64, vcc, s4, v56
	global_load_dwordx4 v[28:31], v[4:5], off offset:-4096 nt
	global_load_dwordx4 v[0:3], v[4:5], off nt
	v_addc_co_u32_e32 v65, vcc, 0, v57, vcc
	global_load_dwordx4 v[4:7], v[12:13], off offset:-4096 nt
	global_load_dwordx4 v[8:11], v[12:13], off nt
	s_nop 0
	global_load_dwordx4 v[12:15], v[20:21], off offset:-4096 nt
	global_load_dwordx4 v[16:19], v[20:21], off nt
	s_nop 0
	global_load_dwordx4 v[20:23], v[32:33], off offset:-4096 nt
	global_load_dwordx4 v[24:27], v[32:33], off nt
	s_nop 0
	global_load_dwordx4 v[32:35], v[40:41], off offset:-4096 nt
	global_load_dwordx4 v[36:39], v[40:41], off nt
	s_nop 0
	global_load_dwordx4 v[40:43], v[48:49], off offset:-4096 nt
	global_load_dwordx4 v[44:47], v[48:49], off nt
	s_nop 0
	global_load_dwordx4 v[48:51], v[58:59], off offset:-4096 nt
	global_load_dwordx4 v[52:55], v[58:59], off nt
	s_nop 0
	global_load_dwordx4 v[56:59], v[64:65], off offset:-4096 nt
	global_load_dwordx4 v[60:63], v[64:65], off nt
	s_lshl_b32 s13, s6, 5
	s_add_u32 s14, s10, 0x2900000
	v_readlane_b32 s6, v243, 0
	s_addc_u32 s15, s11, 0
	s_mov_b32 s8, s6
	s_lshl_b32 s4, s6, 5
	s_lshl_b32 s6, s94, 2
	s_add_i32 s4, s4, s6
	s_lshl_b32 s6, s38, 5
	s_sub_i32 s16, s4, s6
	s_lshl_b32 s4, s8, 3
	s_add_i32 s4, s94, s4
	s_lshl_b32 s6, s38, 3
	s_sub_i32 s4, s4, s6
	v_ashrrev_i32_e32 v133, 31, v132
	s_add_i32 s17, s4, 0x3c0
	s_movk_i32 s18, 0x2000
	s_movk_i32 s19, 0x4000
	s_movk_i32 s20, 0x6000
	s_mov_b32 s21, 0x8000
	s_mov_b32 s22, 0xa000
	s_mov_b32 s23, 0xb000
	s_mov_b32 s24, 0xc000
	s_mov_b32 s25, 0xc3e00000
	v_mov_b32_e32 v135, 0x43e00000
	v_readlane_b32 s7, v243, 1
	s_branch .LBB0_261

.LBB0_259:
	s_nop 1
	v_mul_f32_e32 v128, 0x42000000, v109
	v_mul_f32_e32 v129, 0x42000000, v69
	v_med3_f32 v131, v128, s25, v135
	v_med3_f32 v129, v129, s25, v135
	v_mov_b32_e32 v128, v137
	v_cvt_pk_fp8_f32 v128, v131, v129
	v_mul_f32_e32 v130, 0x42000000, v65
	v_mul_f32_e32 v129, 0x42000000, v77
	v_med3_f32 v130, v130, s25, v135
	v_med3_f32 v129, v129, s25, v135
	v_cvt_pk_fp8_f32 v128, v130, v129 op_sel:[0,0,1]
	v_mul_f32_e32 v129, 0x42000000, v73
	v_mul_f32_e32 v130, 0x42000000, v85
	v_med3_f32 v136, v129, s25, v135
	v_med3_f32 v130, v130, s25, v135
	v_mov_b32_e32 v129, v137
	v_cvt_pk_fp8_f32 v129, v136, v130
	v_mul_f32_e32 v131, 0x42000000, v81
	v_mul_f32_e32 v130, 0x42000000, v93
	v_med3_f32 v131, v131, s25, v135
	v_med3_f32 v130, v130, s25, v135
	v_cvt_pk_fp8_f32 v129, v131, v130 op_sel:[0,0,1]
	v_mul_f32_e32 v130, 0x42000000, v89
	v_mul_f32_e32 v131, 0x42000000, v101
	v_med3_f32 v143, v130, s25, v135
	v_med3_f32 v131, v131, s25, v135
	v_mov_b32_e32 v130, v137
	v_cvt_pk_fp8_f32 v130, v143, v131
	v_mul_f32_e32 v136, 0x42000000, v97
	v_mul_f32_e32 v131, 0x42000000, v105
	v_med3_f32 v136, v136, s25, v135
	v_med3_f32 v131, v131, s25, v135
	v_cvt_pk_fp8_f32 v130, v136, v131 op_sel:[0,0,1]
	v_mul_f32_e32 v131, 0x42000000, v113
	v_mul_f32_e32 v136, 0x42000000, v117
	v_med3_f32 v144, v131, s25, v135
	v_med3_f32 v136, v136, s25, v135
	v_mov_b32_e32 v131, v137
	v_cvt_pk_fp8_f32 v131, v144, v136
	v_mul_f32_e32 v143, 0x42000000, v121
	v_mul_f32_e32 v136, 0x42000000, v125
	v_med3_f32 v143, v143, s25, v135
	v_med3_f32 v136, v136, s25, v135
	v_cvt_pk_fp8_f32 v131, v143, v136 op_sel:[0,0,1]
	v_mul_f32_e32 v136, 0x42000000, v110
	v_mul_f32_e32 v143, 0x42000000, v70
	v_med3_f32 v136, v136, s25, v135
	v_med3_f32 v143, v143, s25, v135
	v_mov_b32_e32 v144, v137
	v_cvt_pk_fp8_f32 v144, v136, v143
	v_mul_f32_e32 v145, 0x42000000, v66
	v_mul_f32_e32 v136, 0x42000000, v78
	v_med3_f32 v143, v145, s25, v135
	v_med3_f32 v136, v136, s25, v135
	v_cvt_pk_fp8_f32 v144, v143, v136 op_sel:[0,0,1]
	v_mul_f32_e32 v136, 0x42000000, v74
	v_mul_f32_e32 v143, 0x42000000, v86
	v_med3_f32 v136, v136, s25, v135
	v_med3_f32 v143, v143, s25, v135
	v_mov_b32_e32 v145, v137
	v_cvt_pk_fp8_f32 v145, v136, v143
	v_mul_f32_e32 v146, 0x42000000, v82
	v_mul_f32_e32 v136, 0x42000000, v94
	v_med3_f32 v143, v146, s25, v135
	v_med3_f32 v136, v136, s25, v135
	v_cvt_pk_fp8_f32 v145, v143, v136 op_sel:[0,0,1]
	v_mul_f32_e32 v136, 0x42000000, v90
	v_mul_f32_e32 v143, 0x42000000, v102
	v_med3_f32 v136, v136, s25, v135
	v_med3_f32 v143, v143, s25, v135
	v_mov_b32_e32 v146, v137
	v_cvt_pk_fp8_f32 v146, v136, v143
	v_mul_f32_e32 v147, 0x42000000, v98
	v_mul_f32_e32 v136, 0x42000000, v106
	v_med3_f32 v143, v147, s25, v135
	v_med3_f32 v136, v136, s25, v135
	v_cvt_pk_fp8_f32 v146, v143, v136 op_sel:[0,0,1]
	v_mul_f32_e32 v136, 0x42000000, v114
	v_mul_f32_e32 v143, 0x42000000, v118
	v_med3_f32 v136, v136, s25, v135
	v_med3_f32 v143, v143, s25, v135
	v_mov_b32_e32 v147, v137
	v_cvt_pk_fp8_f32 v147, v136, v143
	v_mul_f32_e32 v148, 0x42000000, v122
	v_mul_f32_e32 v136, 0x42000000, v126
	v_med3_f32 v143, v148, s25, v135
	v_med3_f32 v136, v136, s25, v135
	v_cvt_pk_fp8_f32 v147, v143, v136 op_sel:[0,0,1]
	v_lshl_add_u64 v[148:149], v[140:141], 0, s[8:9]
	global_store_dwordx4 v[148:149], v[128:131], off
	s_addk_i32 s13, 0x5000
	s_addk_i32 s17, 0x280
	v_lshl_add_u64 v[128:129], v[140:141], 0, s[6:7]
	global_store_dwordx4 v[128:129], v[144:147], off
	v_mul_f32_e32 v128, 0x42000000, v111
	v_mul_f32_e32 v129, 0x42000000, v71
	v_med3_f32 v131, v128, s25, v135
	v_med3_f32 v129, v129, s25, v135
	v_mov_b32_e32 v128, v137
	v_cvt_pk_fp8_f32 v128, v131, v129
	v_mul_f32_e32 v130, 0x42000000, v67
	v_mul_f32_e32 v129, 0x42000000, v79
	v_med3_f32 v130, v130, s25, v135
	v_med3_f32 v129, v129, s25, v135
	v_cvt_pk_fp8_f32 v128, v130, v129 op_sel:[0,0,1]
	v_mul_f32_e32 v129, 0x42000000, v75
	v_mul_f32_e32 v130, 0x42000000, v87
	v_med3_f32 v136, v129, s25, v135
	v_med3_f32 v130, v130, s25, v135
	v_mov_b32_e32 v129, v137
	v_cvt_pk_fp8_f32 v129, v136, v130
	v_mul_f32_e32 v131, 0x42000000, v83
	v_mul_f32_e32 v130, 0x42000000, v95
	v_med3_f32 v131, v131, s25, v135
	v_med3_f32 v130, v130, s25, v135
	v_cvt_pk_fp8_f32 v129, v131, v130 op_sel:[0,0,1]
	v_mul_f32_e32 v130, 0x42000000, v91
	v_mul_f32_e32 v131, 0x42000000, v103
	v_med3_f32 v140, v130, s25, v135
	v_med3_f32 v131, v131, s25, v135
	v_mov_b32_e32 v130, v137
	v_cvt_pk_fp8_f32 v130, v140, v131
	v_mul_f32_e32 v136, 0x42000000, v99
	v_mul_f32_e32 v131, 0x42000000, v107
	v_med3_f32 v136, v136, s25, v135
	v_med3_f32 v131, v131, s25, v135
	v_cvt_pk_fp8_f32 v130, v136, v131 op_sel:[0,0,1]
	v_mul_f32_e32 v131, 0x42000000, v115
	v_mul_f32_e32 v136, 0x42000000, v119
	v_med3_f32 v141, v131, s25, v135
	v_med3_f32 v136, v136, s25, v135
	v_mov_b32_e32 v131, v137
	v_cvt_pk_fp8_f32 v131, v141, v136
	v_mul_f32_e32 v140, 0x42000000, v123
	v_mul_f32_e32 v136, 0x42000000, v127
	v_med3_f32 v140, v140, s25, v135
	v_med3_f32 v136, v136, s25, v135
	v_cvt_pk_fp8_f32 v131, v140, v136 op_sel:[0,0,1]
	v_or_b32_e32 v136, s4, v142
	v_lshlrev_b32_e32 v136, 10, v136
	v_lshl_add_u64 v[138:139], v[138:139], 0, v[136:137]
	s_cmpk_gt_i32 s26, 0x2d7f
	global_store_dwordx4 v[138:139], v[128:131], off
	s_cselect_b64 s[6:7], -1, 0

.LBB0_261:
	s_add_i32 s26, s17, 0xfffffd80
	s_add_i32 s27, s17, 0xfffffec0
	s_cmpk_lt_i32 s26, 0x2ec0
	s_cselect_b64 s[6:7], -1, 0
	s_cmpk_gt_i32 s26, 0x2ebf
	s_cbranch_scc1 .LBB0_263
	s_bitcmp0_b32 s27, 8
	s_cselect_b32 s4, s12, 0x108
	s_add_u32 s8, s0, s4
	s_addc_u32 s9, s1, 0
	s_load_dwordx2 s[8:9], s[8:9], 0x0
	s_lshr_b32 s4, s27, 9
	s_add_i32 s4, s4, 20
	s_lshl_b64 s[10:11], s[4:5], 22
	v_lshlrev_b32_e32 v136, 2, v134
	s_waitcnt lgkmcnt(0)
	s_add_u32 s8, s8, s10
	s_addc_u32 s9, s9, s11
	s_add_i32 s4, s16, 0xa00
	s_and_b32 s4, s4, 0x380
	v_add_u32_e32 v64, s4, v132
	v_ashrrev_i32_e32 v65, 31, v64
	s_and_b32 s10, s13, 0x3e0
	v_lshlrev_b64 v[64:65], 12, v[64:65]
	v_lshl_add_u64 v[64:65], s[8:9], 0, v[64:65]
	s_lshl_b32 s4, s10, 2
	v_lshl_add_u64 v[64:65], v[64:65], 0, s[4:5]
	v_lshl_add_u64 v[120:121], v[64:65], 0, v[136:137]
	v_add_co_u32_e32 v72, vcc, s18, v120
	s_nop 1
	v_addc_co_u32_e32 v73, vcc, 0, v121, vcc
	v_add_co_u32_e32 v80, vcc, s19, v120
	global_load_dwordx4 v[68:71], v[72:73], off offset:-4096 nt
	global_load_dwordx4 v[64:67], v[72:73], off nt
	v_addc_co_u32_e32 v81, vcc, 0, v121, vcc
	v_add_co_u32_e32 v88, vcc, s20, v120
	global_load_dwordx4 v[76:79], v[80:81], off offset:-4096 nt
	global_load_dwordx4 v[72:75], v[80:81], off nt
	v_addc_co_u32_e32 v89, vcc, 0, v121, vcc
	v_add_co_u32_e32 v96, vcc, s21, v120
	global_load_dwordx4 v[84:87], v[88:89], off offset:-4096 nt
	global_load_dwordx4 v[80:83], v[88:89], off nt
	v_addc_co_u32_e32 v97, vcc, 0, v121, vcc
	v_add_co_u32_e32 v104, vcc, s22, v120
	global_load_dwordx4 v[92:95], v[96:97], off offset:-4096 nt
	global_load_dwordx4 v[88:91], v[96:97], off nt
	v_addc_co_u32_e32 v105, vcc, 0, v121, vcc
	v_add_co_u32_e32 v112, vcc, s23, v120
	global_load_dwordx4 v[100:103], v[104:105], off offset:-4096 nt
	global_load_dwordx4 v[96:99], v[104:105], off nt
	v_addc_co_u32_e32 v113, vcc, 0, v121, vcc
	global_load_dwordx4 v[108:111], v[120:121], off nt
	global_load_dwordx4 v[104:107], v[112:113], off nt
	v_add_co_u32_e32 v112, vcc, 0xc000, v120
	s_nop 1
	v_addc_co_u32_e32 v113, vcc, 0, v121, vcc
	v_add_co_u32_e32 v116, vcc, 0xd000, v120
	s_nop 1
	v_addc_co_u32_e32 v117, vcc, 0, v121, vcc
	v_add_co_u32_e32 v122, vcc, 0xe000, v120
	global_load_dwordx4 v[112:115], v[112:113], off nt
	s_nop 0
	global_load_dwordx4 v[116:119], v[116:117], off nt
	v_addc_co_u32_e32 v123, vcc, 0, v121, vcc
	v_add_co_u32_e32 v124, vcc, 0xf000, v120
	s_nop 1
	v_addc_co_u32_e32 v125, vcc, 0, v121, vcc
	global_load_dwordx4 v[120:123], v[122:123], off nt
	s_nop 0
	global_load_dwordx4 v[124:127], v[124:125], off nt

.LBB0_268:
	s_nop 0
	v_mul_f32_e32 v128, 0x42000000, v29
	v_mul_f32_e32 v129, 0x42000000, v1
	v_med3_f32 v131, v128, s25, v135
	v_med3_f32 v129, v129, s25, v135
	v_mov_b32_e32 v128, v137
	v_cvt_pk_fp8_f32 v128, v131, v129
	v_mul_f32_e32 v130, 0x42000000, v5
	v_mul_f32_e32 v129, 0x42000000, v9
	v_med3_f32 v130, v130, s25, v135
	v_med3_f32 v129, v129, s25, v135
	v_cvt_pk_fp8_f32 v128, v130, v129 op_sel:[0,0,1]
	v_mul_f32_e32 v129, 0x42000000, v13
	v_mul_f32_e32 v130, 0x42000000, v17
	v_med3_f32 v143, v129, s25, v135
	v_med3_f32 v130, v130, s25, v135
	v_mov_b32_e32 v129, v137
	v_cvt_pk_fp8_f32 v129, v143, v130
	v_mul_f32_e32 v131, 0x42000000, v21
	v_mul_f32_e32 v130, 0x42000000, v25
	v_med3_f32 v131, v131, s25, v135
	v_med3_f32 v130, v130, s25, v135
	v_cvt_pk_fp8_f32 v129, v131, v130 op_sel:[0,0,1]
	v_mul_f32_e32 v130, 0x42000000, v33
	v_mul_f32_e32 v131, 0x42000000, v37
	v_med3_f32 v144, v130, s25, v135
	v_med3_f32 v131, v131, s25, v135
	v_mov_b32_e32 v130, v137
	v_cvt_pk_fp8_f32 v130, v144, v131
	v_mul_f32_e32 v143, 0x42000000, v41
	v_mul_f32_e32 v131, 0x42000000, v45
	v_med3_f32 v143, v143, s25, v135
	v_med3_f32 v131, v131, s25, v135
	v_cvt_pk_fp8_f32 v130, v143, v131 op_sel:[0,0,1]
	v_mul_f32_e32 v131, 0x42000000, v49
	v_mul_f32_e32 v143, 0x42000000, v53
	v_med3_f32 v145, v131, s25, v135
	v_med3_f32 v143, v143, s25, v135
	v_mov_b32_e32 v131, v137
	v_cvt_pk_fp8_f32 v131, v145, v143
	v_mul_f32_e32 v144, 0x42000000, v57
	v_mul_f32_e32 v143, 0x42000000, v61
	v_med3_f32 v144, v144, s25, v135
	v_med3_f32 v143, v143, s25, v135
	v_cvt_pk_fp8_f32 v131, v144, v143 op_sel:[0,0,1]
	v_mul_f32_e32 v143, 0x42000000, v30
	v_mul_f32_e32 v144, 0x42000000, v2
	v_med3_f32 v143, v143, s25, v135
	v_med3_f32 v146, v144, s25, v135
	v_mov_b32_e32 v144, v137
	v_cvt_pk_fp8_f32 v144, v143, v146
	v_mul_f32_e32 v145, 0x42000000, v6
	v_mul_f32_e32 v143, 0x42000000, v10
	v_med3_f32 v145, v145, s25, v135
	v_med3_f32 v143, v143, s25, v135
	v_cvt_pk_fp8_f32 v144, v145, v143 op_sel:[0,0,1]
	v_mul_f32_e32 v143, 0x42000000, v14
	v_mul_f32_e32 v145, 0x42000000, v18
	v_med3_f32 v143, v143, s25, v135
	v_med3_f32 v147, v145, s25, v135
	v_mov_b32_e32 v145, v137
	v_cvt_pk_fp8_f32 v145, v143, v147
	v_mul_f32_e32 v146, 0x42000000, v22
	v_mul_f32_e32 v143, 0x42000000, v26
	v_med3_f32 v146, v146, s25, v135
	v_med3_f32 v143, v143, s25, v135
	v_cvt_pk_fp8_f32 v145, v146, v143 op_sel:[0,0,1]
	v_mul_f32_e32 v143, 0x42000000, v34
	v_mul_f32_e32 v146, 0x42000000, v38
	v_med3_f32 v143, v143, s25, v135
	v_med3_f32 v148, v146, s25, v135
	v_mov_b32_e32 v146, v137
	v_cvt_pk_fp8_f32 v146, v143, v148
	v_mul_f32_e32 v147, 0x42000000, v42
	v_mul_f32_e32 v143, 0x42000000, v46
	v_med3_f32 v147, v147, s25, v135
	v_med3_f32 v143, v143, s25, v135
	v_cvt_pk_fp8_f32 v146, v147, v143 op_sel:[0,0,1]
	v_mul_f32_e32 v143, 0x42000000, v50
	v_mul_f32_e32 v147, 0x42000000, v54
	v_med3_f32 v143, v143, s25, v135
	v_med3_f32 v149, v147, s25, v135
	v_mov_b32_e32 v147, v137
	v_cvt_pk_fp8_f32 v147, v143, v149
	v_mul_f32_e32 v148, 0x42000000, v58
	v_mul_f32_e32 v143, 0x42000000, v62
	v_med3_f32 v148, v148, s25, v135
	v_med3_f32 v143, v143, s25, v135
	v_cvt_pk_fp8_f32 v147, v148, v143 op_sel:[0,0,1]
	v_lshl_add_u64 v[148:149], v[140:141], 0, s[10:11]
	global_store_dwordx4 v[148:149], v[128:131], off
	s_andn2_b64 vcc, exec, s[6:7]
	s_mov_b64 s[6:7], -1
	v_lshl_add_u64 v[128:129], v[140:141], 0, s[8:9]
	global_store_dwordx4 v[128:129], v[144:147], off
	v_mul_f32_e32 v128, 0x42000000, v31
	v_mul_f32_e32 v129, 0x42000000, v3
	v_med3_f32 v131, v128, s25, v135
	v_med3_f32 v129, v129, s25, v135
	v_mov_b32_e32 v128, v137
	v_cvt_pk_fp8_f32 v128, v131, v129
	v_mul_f32_e32 v130, 0x42000000, v7
	v_mul_f32_e32 v129, 0x42000000, v11
	v_med3_f32 v130, v130, s25, v135
	v_med3_f32 v129, v129, s25, v135
	v_cvt_pk_fp8_f32 v128, v130, v129 op_sel:[0,0,1]
	v_mul_f32_e32 v129, 0x42000000, v15
	v_mul_f32_e32 v130, 0x42000000, v19
	v_med3_f32 v140, v129, s25, v135
	v_med3_f32 v130, v130, s25, v135
	v_mov_b32_e32 v129, v137
	v_cvt_pk_fp8_f32 v129, v140, v130
	v_mul_f32_e32 v131, 0x42000000, v23
	v_mul_f32_e32 v130, 0x42000000, v27
	v_med3_f32 v131, v131, s25, v135
	v_med3_f32 v130, v130, s25, v135
	v_cvt_pk_fp8_f32 v129, v131, v130 op_sel:[0,0,1]
	v_mul_f32_e32 v130, 0x42000000, v35
	v_mul_f32_e32 v131, 0x42000000, v39
	v_med3_f32 v141, v130, s25, v135
	v_med3_f32 v131, v131, s25, v135
	v_mov_b32_e32 v130, v137
	v_cvt_pk_fp8_f32 v130, v141, v131
	v_mul_f32_e32 v140, 0x42000000, v43
	v_mul_f32_e32 v131, 0x42000000, v47
	v_med3_f32 v140, v140, s25, v135
	v_med3_f32 v131, v131, s25, v135
	v_cvt_pk_fp8_f32 v130, v140, v131 op_sel:[0,0,1]
	v_mul_f32_e32 v131, 0x42000000, v51
	v_mul_f32_e32 v140, 0x42000000, v55
	v_med3_f32 v143, v131, s25, v135
	v_med3_f32 v140, v140, s25, v135
	v_mov_b32_e32 v131, v137
	v_cvt_pk_fp8_f32 v131, v143, v140
	v_mul_f32_e32 v141, 0x42000000, v59
	v_mul_f32_e32 v140, 0x42000000, v63
	v_med3_f32 v141, v141, s25, v135
	v_med3_f32 v140, v140, s25, v135
	v_cvt_pk_fp8_f32 v131, v141, v140 op_sel:[0,0,1]
	v_or_b32_e32 v140, s4, v142
	v_lshlrev_b32_e32 v140, 10, v140
	v_mov_b32_e32 v141, v137
	v_lshl_add_u64 v[138:139], v[138:139], 0, v[140:141]
	global_store_dwordx4 v[138:139], v[128:131], off
	s_cbranch_vccnz .LBB0_260
	s_cmpk_gt_i32 s26, 0x2d7f
	s_cbranch_scc1 .LBB0_271
	s_bitcmp0_b32 s17, 8
	s_cselect_b32 s4, s12, 0x108
	s_add_u32 s6, s0, s4
	s_addc_u32 s7, s1, 0
	s_load_dwordx2 s[6:7], s[6:7], 0x0
	s_lshr_b32 s4, s17, 9
	s_add_i32 s4, s4, 20
	s_lshl_b64 s[8:9], s[4:5], 22
	v_lshlrev_b32_e32 v2, 2, v134
	s_waitcnt lgkmcnt(0)
	s_add_u32 s6, s6, s8
	s_addc_u32 s7, s7, s9
	s_add_i32 s4, s16, 0xf00
	s_and_b32 s4, s4, 0x380
	v_add_u32_e32 v0, s4, v132
	v_ashrrev_i32_e32 v1, 31, v0
	s_and_b32 s8, s13, 0x3e0
	v_lshlrev_b64 v[0:1], 12, v[0:1]
	v_lshl_add_u64 v[0:1], s[6:7], 0, v[0:1]
	s_lshl_b32 s4, s8, 2
	v_lshl_add_u64 v[0:1], v[0:1], 0, s[4:5]
	v_mov_b32_e32 v3, v137
	v_lshl_add_u64 v[56:57], v[0:1], 0, v[2:3]
	v_add_co_u32_e32 v8, vcc, s18, v56
	s_nop 1
	v_addc_co_u32_e32 v9, vcc, 0, v57, vcc
	v_add_co_u32_e32 v16, vcc, s19, v56
	global_load_dwordx4 v[0:3], v[8:9], off offset:-4096 nt
	global_load_dwordx4 v[4:7], v[8:9], off nt
	v_addc_co_u32_e32 v17, vcc, 0, v57, vcc
	v_add_co_u32_e32 v24, vcc, s20, v56
	global_load_dwordx4 v[8:11], v[16:17], off offset:-4096 nt
	global_load_dwordx4 v[12:15], v[16:17], off nt
	v_addc_co_u32_e32 v25, vcc, 0, v57, vcc
	v_add_co_u32_e32 v28, vcc, s21, v56
	global_load_dwordx4 v[16:19], v[24:25], off offset:-4096 nt
	global_load_dwordx4 v[20:23], v[24:25], off nt
	v_addc_co_u32_e32 v29, vcc, 0, v57, vcc
	global_load_dwordx4 v[24:27], v[28:29], off offset:-4096 nt
	global_load_dwordx4 v[32:35], v[28:29], off nt
	v_add_co_u32_e32 v28, vcc, s22, v56
	s_nop 1
	v_addc_co_u32_e32 v29, vcc, 0, v57, vcc
	global_load_dwordx4 v[36:39], v[28:29], off offset:-4096 nt
	global_load_dwordx4 v[40:43], v[28:29], off nt
	v_add_co_u32_e32 v28, vcc, s24, v56
	s_nop 1
	v_addc_co_u32_e32 v29, vcc, 0, v57, vcc
	v_add_co_u32_e32 v52, vcc, 0xd000, v56
	global_load_dwordx4 v[44:47], v[28:29], off offset:-4096 nt
	global_load_dwordx4 v[48:51], v[28:29], off nt
	v_addc_co_u32_e32 v53, vcc, 0, v57, vcc
	v_add_co_u32_e32 v58, vcc, 0xe000, v56
	global_load_dwordx4 v[28:31], v[56:57], off nt
	s_nop 0
	global_load_dwordx4 v[52:55], v[52:53], off nt
	v_addc_co_u32_e32 v59, vcc, 0, v57, vcc
	v_add_co_u32_e32 v60, vcc, 0xf000, v56
	s_nop 1
	v_addc_co_u32_e32 v61, vcc, 0, v57, vcc
	global_load_dwordx4 v[56:59], v[58:59], off nt
	s_nop 0
	global_load_dwordx4 v[60:63], v[60:61], off nt
